# speedup vs baseline: 1.0519x; 1.0483x over previous
.Lp_main:
	s_load_dwordx2 s[10:11], s[0:1], 0x0
	s_load_dwordx4 s[12:15], s[0:1], 0x10
	s_load_dwordx2 s[16:17], s[0:1], 0x20
	s_load_dwordx4 s[20:23], s[0:1], 0x28
	v_readfirstlane_b32 s3, v0
	v_and_b32_e32 v154, 63, v0
	v_lshrrev_b32_e32 v155, 5, v154
	v_lshlrev_b32_e32 v156, 4, v0
	v_lshlrev_b32_e32 v157, 4, v154
	v_lshlrev_b32_e32 v158, 8, v1
	v_lshl_add_u32 v158, v155, 5, v158
	v_lshlrev_b32_e32 v159, 4, v155
	v_lshrrev_b32_e32 v160, 3, v0
	v_lshlrev_b32_e32 v160, 12, v160
	v_and_b32_e32 v161, 7, v0
	v_lshl_add_u32 v160, v161, 4, v160
	s_lshr_b32 s41, s2, 3
	s_and_b32 s42, s2, 7
	s_lshl_b32 s24, s42, 2
	s_bfe_u32 s25, s2, 0x20003
	s_add_u32 s24, s24, s25
	s_lshr_b32 s25, s2, 5
	s_lshr_b32 s26, s3, 6
	s_lshl_b32 s27, s25, 2
	s_add_u32 s27, s27, s26
	s_mov_b32 s4, 0x4038aa3b
	s_mov_b32 s5, s4
	s_lshl_b32 s40, s26, 6
	s_waitcnt lgkmcnt(0)
	s_lshl_b32 s28, s24, 15
	s_add_u32 s28, s28, 0x1000
	s_add_u32 s10, s10, s28
	s_addc_u32 s11, s11, 0
	s_lshl_b32 s34, s41, 17
	s_lshl_b32 s35, s42, 9
	s_add_u32 s34, s34, s35
	s_add_u32 s34, s14, s34
	s_addc_u32 s35, s15, 0
	s_lshl_b32 s28, s27, 13
	s_add_u32 s28, s8, s28
	s_addc_u32 s29, s9, 0
	s_lshl_b32 s30, s27, 7
	s_add_u32 s30, s12, s30
	s_addc_u32 s31, s13, 0
	global_load_dwordx4 v[2:5], v156, s[10:11] offset:-4096
	global_load_dwordx4 v[6:9], v156, s[10:11] offset:0
	s_add_u32 s10, s10, 0x2000
	s_addc_u32 s11, s11, 0
	global_load_dwordx4 v[10:13], v156, s[10:11] offset:-4096
	global_load_dwordx4 v[14:17], v156, s[10:11] offset:0
	s_add_u32 s10, s10, 0x2000
	s_addc_u32 s11, s11, 0
	global_load_dwordx4 v[18:21], v156, s[10:11] offset:-4096
	global_load_dwordx4 v[22:25], v156, s[10:11] offset:0
	s_add_u32 s10, s10, 0x2000
	s_addc_u32 s11, s11, 0
	global_load_dwordx4 v[26:29], v156, s[10:11] offset:-4096
	global_load_dwordx4 v[30:33], v156, s[10:11] offset:0
	global_load_dwordx4 v[34:37], v158, s[28:29] offset:0
	global_load_dwordx4 v[38:41], v158, s[28:29] offset:16
	global_load_dwordx4 v[42:45], v158, s[28:29] offset:64
	global_load_dwordx4 v[46:49], v158, s[28:29] offset:80
	global_load_dwordx4 v[50:53], v158, s[28:29] offset:128
	global_load_dwordx4 v[54:57], v158, s[28:29] offset:144
	global_load_dwordx4 v[58:61], v158, s[28:29] offset:192
	global_load_dwordx4 v[62:65], v158, s[28:29] offset:208
	global_load_dwordx4 v[66:69], v159, s[30:31] offset:0
	global_load_dwordx4 v[70:73], v159, s[30:31] offset:32
	global_load_dwordx4 v[74:77], v159, s[30:31] offset:64
	global_load_dwordx4 v[78:81], v159, s[30:31] offset:96
	global_load_dwordx4 v[168:171], v160, s[34:35] offset:0
	global_load_dwordx4 v[172:175], v160, s[34:35] offset:128
	global_load_dwordx4 v[176:179], v160, s[34:35] offset:256
	global_load_dwordx4 v[180:183], v160, s[34:35] offset:384
	v_bfe_u32 v163, v0, 1, 3
	v_mul_u32_u24_e32 v163, 0x210, v163
	v_lshrrev_b32_e32 v164, 4, v0
	v_lshl_add_u32 v163, v164, 4, v163
	v_and_b32_e32 v164, 1, v0
	v_lshl_add_u32 v163, v164, 3, v163
	v_lshrrev_b32_e32 v164, 3, v0
	v_mul_u32_u24_e32 v164, 0x110, v164
	v_lshl_add_u32 v164, v161, 3, v164
	v_add_u32_e32 v164, 0x4200, v164
	v_mul_u32_u24_e32 v165, 0x210, v155
	v_lshl_add_u32 v165, v1, 4, v165
	v_mul_u32_u24_e32 v166, 0x110, v1
	v_lshl_add_u32 v166, v155, 4, v166
	v_add_u32_e32 v166, s40, v166
	v_add_u32_e32 v166, 0x4200, v166
	v_mul_u32_u24_e32 v167, 0x880, v155
	v_lshl_add_u32 v167, v1, 1, v167
	v_add_u32_e32 v167, s40, v167
	v_add_u32_e32 v167, 0x4200, v167
	s_lshl_b32 s32, s24, 18
	s_lshl_b32 s33, s27, 11
	s_add_u32 s32, s32, s33
	s_add_u32 s32, s16, s32
	s_addc_u32 s33, s17, 0
	s_lshl_b32 s36, s41, 16
	s_lshl_b32 s37, s42, 13
	s_add_u32 s36, s36, s37
	s_lshl_b32 s37, s26, 11
	s_add_u32 s36, s36, s37
	s_add_u32 s36, s20, s36
	s_addc_u32 s37, s21, 0
	s_lshl_b32 s38, s42, 18
	s_lshl_b32 s39, s26, 16
	s_add_u32 s38, s38, s39
	s_lshl_b32 s39, s41, 11
	s_add_u32 s38, s38, s39
	s_add_u32 s38, s22, s38
	s_addc_u32 s39, s23, 0
	s_waitcnt vmcnt(23)
	v_cvt_pk_f16_f32 v2, v2, v3
	v_cvt_pk_f16_f32 v3, v4, v5
	ds_write_b64 v163, v[2:3] offset:0
	s_waitcnt vmcnt(22)
	v_cvt_pk_f16_f32 v6, v6, v7
	v_cvt_pk_f16_f32 v7, v8, v9
	ds_write_b64 v163, v[6:7] offset:256
	s_waitcnt vmcnt(21)
	v_cvt_pk_f16_f32 v10, v10, v11
	v_cvt_pk_f16_f32 v11, v12, v13
	ds_write_b64 v163, v[10:11] offset:4224
	s_waitcnt vmcnt(20)
	v_cvt_pk_f16_f32 v14, v14, v15
	v_cvt_pk_f16_f32 v15, v16, v17
	ds_write_b64 v163, v[14:15] offset:4480
	s_waitcnt vmcnt(19)
	v_cvt_pk_f16_f32 v18, v18, v19
	v_cvt_pk_f16_f32 v19, v20, v21
	ds_write_b64 v163, v[18:19] offset:8448
	s_waitcnt vmcnt(18)
	v_cvt_pk_f16_f32 v22, v22, v23
	v_cvt_pk_f16_f32 v23, v24, v25
	ds_write_b64 v163, v[22:23] offset:8704
	s_waitcnt vmcnt(17)
	v_cvt_pk_f16_f32 v26, v26, v27
	v_cvt_pk_f16_f32 v27, v28, v29
	ds_write_b64 v163, v[26:27] offset:12672
	s_waitcnt vmcnt(16)
	v_cvt_pk_f16_f32 v30, v30, v31
	v_cvt_pk_f16_f32 v31, v32, v33
	ds_write_b64 v163, v[30:31] offset:12928
	s_waitcnt lgkmcnt(0)
	s_barrier
	ds_read_b128 v[2:5], v165 offset:0
	ds_read_b128 v[6:9], v165 offset:1056
	ds_read_b128 v[10:13], v165 offset:2112
	ds_read_b128 v[14:17], v165 offset:3168
	ds_read_b128 v[18:21], v165 offset:4224
	ds_read_b128 v[22:25], v165 offset:5280
	ds_read_b128 v[26:29], v165 offset:6336
	ds_read_b128 v[30:33], v165 offset:7392
	s_waitcnt vmcnt(8)
	v_cvt_pk_f16_f32 v82, v34, v35
	v_cvt_pk_f16_f32 v83, v36, v37
	v_cvt_pk_f16_f32 v84, v38, v39
	v_cvt_pk_f16_f32 v85, v40, v41
	v_cvt_pk_f16_f32 v86, v42, v43
	v_cvt_pk_f16_f32 v87, v44, v45
	v_cvt_pk_f16_f32 v88, v46, v47
	v_cvt_pk_f16_f32 v89, v48, v49
	v_cvt_pk_f16_f32 v90, v50, v51
	v_cvt_pk_f16_f32 v91, v52, v53
	v_cvt_pk_f16_f32 v92, v54, v55
	v_cvt_pk_f16_f32 v93, v56, v57
	v_cvt_pk_f16_f32 v94, v58, v59
	v_cvt_pk_f16_f32 v95, v60, v61
	v_cvt_pk_f16_f32 v96, v62, v63
	v_cvt_pk_f16_f32 v97, v64, v65
	ds_read_b128 v[34:37], v165 offset:8448
	ds_read_b128 v[38:41], v165 offset:9504
	ds_read_b128 v[42:45], v165 offset:10560
	ds_read_b128 v[46:49], v165 offset:11616
	s_waitcnt vmcnt(4)
	v_pk_mul_f32 v[66:67], v[66:67], s[4:5] op_sel_hi:[1,0]
	v_pk_mul_f32 v[68:69], v[68:69], s[4:5] op_sel_hi:[1,0]
	v_pk_mul_f32 v[70:71], v[70:71], s[4:5] op_sel_hi:[1,0]
	v_pk_mul_f32 v[72:73], v[72:73], s[4:5] op_sel_hi:[1,0]
	v_pk_mul_f32 v[74:75], v[74:75], s[4:5] op_sel_hi:[1,0]
	v_pk_mul_f32 v[76:77], v[76:77], s[4:5] op_sel_hi:[1,0]
	v_pk_mul_f32 v[78:79], v[78:79], s[4:5] op_sel_hi:[1,0]
	v_pk_mul_f32 v[80:81], v[80:81], s[4:5] op_sel_hi:[1,0]
	s_waitcnt lgkmcnt(8)
	v_mfma_f32_32x32x16_f16 v[98:113], v[82:85], v[2:5], 0
	v_mfma_f32_32x32x16_f16 v[98:113], v[86:89], v[6:9], v[98:113]
	v_mfma_f32_32x32x16_f16 v[98:113], v[90:93], v[10:13], v[98:113]
	v_mfma_f32_32x32x16_f16 v[98:113], v[94:97], v[14:17], v[98:113]
	ds_read_b128 v[50:53], v165 offset:12672
	ds_read_b128 v[54:57], v165 offset:13728
	ds_read_b128 v[58:61], v165 offset:14784
	ds_read_b128 v[62:65], v165 offset:15840
	s_waitcnt lgkmcnt(8)
	v_mfma_f32_32x32x16_f16 v[114:129], v[82:85], v[18:21], 0
	v_mfma_f32_32x32x16_f16 v[114:129], v[86:89], v[22:25], v[114:129]
	v_mfma_f32_32x32x16_f16 v[114:129], v[90:93], v[26:29], v[114:129]
	v_mfma_f32_32x32x16_f16 v[114:129], v[94:97], v[30:33], v[114:129]
	s_nop 7
	v_pk_fma_f32 v[130:131], v[98:99], s[4:5], v[66:67] op_sel_hi:[1,0,1]
	v_pk_fma_f32 v[132:133], v[100:101], s[4:5], v[68:69] op_sel_hi:[1,0,1]
	v_pk_fma_f32 v[134:135], v[102:103], s[4:5], v[70:71] op_sel_hi:[1,0,1]
	v_pk_fma_f32 v[136:137], v[104:105], s[4:5], v[72:73] op_sel_hi:[1,0,1]
	v_pk_fma_f32 v[138:139], v[106:107], s[4:5], v[74:75] op_sel_hi:[1,0,1]
	v_pk_fma_f32 v[140:141], v[108:109], s[4:5], v[76:77] op_sel_hi:[1,0,1]
	v_pk_fma_f32 v[142:143], v[110:111], s[4:5], v[78:79] op_sel_hi:[1,0,1]
	v_pk_fma_f32 v[144:145], v[112:113], s[4:5], v[80:81] op_sel_hi:[1,0,1]
	v_exp_f32_e32 v130, v130
	v_exp_f32_e32 v131, v131
	v_exp_f32_e32 v132, v132
	v_exp_f32_e32 v133, v133
	v_exp_f32_e32 v134, v134
	v_exp_f32_e32 v135, v135
	v_exp_f32_e32 v136, v136
	v_exp_f32_e32 v137, v137
	v_exp_f32_e32 v138, v138
	v_exp_f32_e32 v139, v139
	v_exp_f32_e32 v140, v140
	v_exp_f32_e32 v141, v141
	v_exp_f32_e32 v142, v142
	v_exp_f32_e32 v143, v143
	v_exp_f32_e32 v144, v144
	v_exp_f32_e32 v145, v145
	v_pk_add_f32 v[130:131], v[130:131], 1.0 op_sel_hi:[1,0]
	v_pk_add_f32 v[132:133], v[132:133], 1.0 op_sel_hi:[1,0]
	v_pk_add_f32 v[134:135], v[134:135], 1.0 op_sel_hi:[1,0]
	v_pk_add_f32 v[136:137], v[136:137], 1.0 op_sel_hi:[1,0]
	v_pk_add_f32 v[138:139], v[138:139], 1.0 op_sel_hi:[1,0]
	v_pk_add_f32 v[140:141], v[140:141], 1.0 op_sel_hi:[1,0]
	v_pk_add_f32 v[142:143], v[142:143], 1.0 op_sel_hi:[1,0]
	v_pk_add_f32 v[144:145], v[144:145], 1.0 op_sel_hi:[1,0]
	v_rcp_f32_e32 v130, v130
	v_rcp_f32_e32 v131, v131
	v_rcp_f32_e32 v132, v132
	v_rcp_f32_e32 v133, v133
	v_rcp_f32_e32 v134, v134
	v_rcp_f32_e32 v135, v135
	v_rcp_f32_e32 v136, v136
	v_rcp_f32_e32 v137, v137
	v_rcp_f32_e32 v138, v138
	v_rcp_f32_e32 v139, v139
	v_rcp_f32_e32 v140, v140
	v_rcp_f32_e32 v141, v141
	v_rcp_f32_e32 v142, v142
	v_rcp_f32_e32 v143, v143
	v_rcp_f32_e32 v144, v144
	v_rcp_f32_e32 v145, v145
	v_pk_fma_f32 v[130:131], v[130:131], 2.0, 1.0 op_sel_hi:[1,0,0] neg_lo:[1,0,0] neg_hi:[1,0,0]
	v_pk_fma_f32 v[132:133], v[132:133], 2.0, 1.0 op_sel_hi:[1,0,0] neg_lo:[1,0,0] neg_hi:[1,0,0]
	v_pk_fma_f32 v[134:135], v[134:135], 2.0, 1.0 op_sel_hi:[1,0,0] neg_lo:[1,0,0] neg_hi:[1,0,0]
	v_pk_fma_f32 v[136:137], v[136:137], 2.0, 1.0 op_sel_hi:[1,0,0] neg_lo:[1,0,0] neg_hi:[1,0,0]
	v_pk_fma_f32 v[138:139], v[138:139], 2.0, 1.0 op_sel_hi:[1,0,0] neg_lo:[1,0,0] neg_hi:[1,0,0]
	v_pk_fma_f32 v[140:141], v[140:141], 2.0, 1.0 op_sel_hi:[1,0,0] neg_lo:[1,0,0] neg_hi:[1,0,0]
	v_pk_fma_f32 v[142:143], v[142:143], 2.0, 1.0 op_sel_hi:[1,0,0] neg_lo:[1,0,0] neg_hi:[1,0,0]
	v_pk_fma_f32 v[144:145], v[144:145], 2.0, 1.0 op_sel_hi:[1,0,0] neg_lo:[1,0,0] neg_hi:[1,0,0]
	v_cvt_pk_f16_f32 v146, v130, v131
	v_cvt_pk_f16_f32 v147, v132, v133
	v_cvt_pk_f16_f32 v148, v134, v135
	v_cvt_pk_f16_f32 v149, v136, v137
	v_cvt_pk_f16_f32 v150, v138, v139
	v_cvt_pk_f16_f32 v151, v140, v141
	v_cvt_pk_f16_f32 v152, v142, v143
	v_cvt_pk_f16_f32 v153, v144, v145
	s_nop 1
	v_permlane32_swap_b32_e32 v146, v148
	v_permlane32_swap_b32_e32 v147, v149
	v_permlane32_swap_b32_e32 v150, v152
	v_permlane32_swap_b32_e32 v151, v153
	global_store_dwordx4 v157, v[146:149], s[32:33] sc1
	global_store_dwordx4 v157, v[150:153], s[32:33] offset:1024 sc1
	s_add_u32 s32, s32, 0x10000
	s_addc_u32 s33, s33, 0
	s_waitcnt lgkmcnt(4)
	v_mfma_f32_32x32x16_f16 v[98:113], v[82:85], v[34:37], 0
	v_mfma_f32_32x32x16_f16 v[98:113], v[86:89], v[38:41], v[98:113]
	v_mfma_f32_32x32x16_f16 v[98:113], v[90:93], v[42:45], v[98:113]
	v_mfma_f32_32x32x16_f16 v[98:113], v[94:97], v[46:49], v[98:113]
	v_pk_fma_f32 v[130:131], v[114:115], s[4:5], v[66:67] op_sel_hi:[1,0,1]
	v_pk_fma_f32 v[132:133], v[116:117], s[4:5], v[68:69] op_sel_hi:[1,0,1]
	v_pk_fma_f32 v[134:135], v[118:119], s[4:5], v[70:71] op_sel_hi:[1,0,1]
	v_pk_fma_f32 v[136:137], v[120:121], s[4:5], v[72:73] op_sel_hi:[1,0,1]
	v_pk_fma_f32 v[138:139], v[122:123], s[4:5], v[74:75] op_sel_hi:[1,0,1]
	v_pk_fma_f32 v[140:141], v[124:125], s[4:5], v[76:77] op_sel_hi:[1,0,1]
	v_pk_fma_f32 v[142:143], v[126:127], s[4:5], v[78:79] op_sel_hi:[1,0,1]
	v_pk_fma_f32 v[144:145], v[128:129], s[4:5], v[80:81] op_sel_hi:[1,0,1]
	v_exp_f32_e32 v130, v130
	v_exp_f32_e32 v131, v131
	v_exp_f32_e32 v132, v132
	v_exp_f32_e32 v133, v133
	v_exp_f32_e32 v134, v134
	v_exp_f32_e32 v135, v135
	v_exp_f32_e32 v136, v136
	v_exp_f32_e32 v137, v137
	v_exp_f32_e32 v138, v138
	v_exp_f32_e32 v139, v139
	v_exp_f32_e32 v140, v140
	v_exp_f32_e32 v141, v141
	v_exp_f32_e32 v142, v142
	v_exp_f32_e32 v143, v143
	v_exp_f32_e32 v144, v144
	v_exp_f32_e32 v145, v145
	v_pk_add_f32 v[130:131], v[130:131], 1.0 op_sel_hi:[1,0]
	v_pk_add_f32 v[132:133], v[132:133], 1.0 op_sel_hi:[1,0]
	v_pk_add_f32 v[134:135], v[134:135], 1.0 op_sel_hi:[1,0]
	v_pk_add_f32 v[136:137], v[136:137], 1.0 op_sel_hi:[1,0]
	v_pk_add_f32 v[138:139], v[138:139], 1.0 op_sel_hi:[1,0]
	v_pk_add_f32 v[140:141], v[140:141], 1.0 op_sel_hi:[1,0]
	v_pk_add_f32 v[142:143], v[142:143], 1.0 op_sel_hi:[1,0]
	v_pk_add_f32 v[144:145], v[144:145], 1.0 op_sel_hi:[1,0]
	v_rcp_f32_e32 v130, v130
	v_rcp_f32_e32 v131, v131
	v_rcp_f32_e32 v132, v132
	v_rcp_f32_e32 v133, v133
	v_rcp_f32_e32 v134, v134
	v_rcp_f32_e32 v135, v135
	v_rcp_f32_e32 v136, v136
	v_rcp_f32_e32 v137, v137
	v_rcp_f32_e32 v138, v138
	v_rcp_f32_e32 v139, v139
	v_rcp_f32_e32 v140, v140
	v_rcp_f32_e32 v141, v141
	v_rcp_f32_e32 v142, v142
	v_rcp_f32_e32 v143, v143
	v_rcp_f32_e32 v144, v144
	v_rcp_f32_e32 v145, v145
	v_pk_fma_f32 v[130:131], v[130:131], 2.0, 1.0 op_sel_hi:[1,0,0] neg_lo:[1,0,0] neg_hi:[1,0,0]
	v_pk_fma_f32 v[132:133], v[132:133], 2.0, 1.0 op_sel_hi:[1,0,0] neg_lo:[1,0,0] neg_hi:[1,0,0]
	v_pk_fma_f32 v[134:135], v[134:135], 2.0, 1.0 op_sel_hi:[1,0,0] neg_lo:[1,0,0] neg_hi:[1,0,0]
	v_pk_fma_f32 v[136:137], v[136:137], 2.0, 1.0 op_sel_hi:[1,0,0] neg_lo:[1,0,0] neg_hi:[1,0,0]
	v_pk_fma_f32 v[138:139], v[138:139], 2.0, 1.0 op_sel_hi:[1,0,0] neg_lo:[1,0,0] neg_hi:[1,0,0]
	v_pk_fma_f32 v[140:141], v[140:141], 2.0, 1.0 op_sel_hi:[1,0,0] neg_lo:[1,0,0] neg_hi:[1,0,0]
	v_pk_fma_f32 v[142:143], v[142:143], 2.0, 1.0 op_sel_hi:[1,0,0] neg_lo:[1,0,0] neg_hi:[1,0,0]
	v_pk_fma_f32 v[144:145], v[144:145], 2.0, 1.0 op_sel_hi:[1,0,0] neg_lo:[1,0,0] neg_hi:[1,0,0]
	v_cvt_pk_f16_f32 v146, v130, v131
	v_cvt_pk_f16_f32 v147, v132, v133
	v_cvt_pk_f16_f32 v148, v134, v135
	v_cvt_pk_f16_f32 v149, v136, v137
	v_cvt_pk_f16_f32 v150, v138, v139
	v_cvt_pk_f16_f32 v151, v140, v141
	v_cvt_pk_f16_f32 v152, v142, v143
	v_cvt_pk_f16_f32 v153, v144, v145
	s_nop 1
	v_permlane32_swap_b32_e32 v146, v148
	v_permlane32_swap_b32_e32 v147, v149
	v_permlane32_swap_b32_e32 v150, v152
	v_permlane32_swap_b32_e32 v151, v153
	global_store_dwordx4 v157, v[146:149], s[32:33] sc1
	global_store_dwordx4 v157, v[150:153], s[32:33] offset:1024 sc1
	s_add_u32 s32, s32, 0x10000
	s_addc_u32 s33, s33, 0
	s_waitcnt lgkmcnt(0)
	v_mfma_f32_32x32x16_f16 v[114:129], v[82:85], v[50:53], 0
	v_mfma_f32_32x32x16_f16 v[114:129], v[86:89], v[54:57], v[114:129]
	v_mfma_f32_32x32x16_f16 v[114:129], v[90:93], v[58:61], v[114:129]
	v_mfma_f32_32x32x16_f16 v[114:129], v[94:97], v[62:65], v[114:129]
	v_pk_fma_f32 v[130:131], v[98:99], s[4:5], v[66:67] op_sel_hi:[1,0,1]
	v_pk_fma_f32 v[132:133], v[100:101], s[4:5], v[68:69] op_sel_hi:[1,0,1]
	v_pk_fma_f32 v[134:135], v[102:103], s[4:5], v[70:71] op_sel_hi:[1,0,1]
	v_pk_fma_f32 v[136:137], v[104:105], s[4:5], v[72:73] op_sel_hi:[1,0,1]
	v_pk_fma_f32 v[138:139], v[106:107], s[4:5], v[74:75] op_sel_hi:[1,0,1]
	v_pk_fma_f32 v[140:141], v[108:109], s[4:5], v[76:77] op_sel_hi:[1,0,1]
	v_pk_fma_f32 v[142:143], v[110:111], s[4:5], v[78:79] op_sel_hi:[1,0,1]
	v_pk_fma_f32 v[144:145], v[112:113], s[4:5], v[80:81] op_sel_hi:[1,0,1]
	v_exp_f32_e32 v130, v130
	v_exp_f32_e32 v131, v131
	v_exp_f32_e32 v132, v132
	v_exp_f32_e32 v133, v133
	v_exp_f32_e32 v134, v134
	v_exp_f32_e32 v135, v135
	v_exp_f32_e32 v136, v136
	v_exp_f32_e32 v137, v137
	v_exp_f32_e32 v138, v138
	v_exp_f32_e32 v139, v139
	v_exp_f32_e32 v140, v140
	v_exp_f32_e32 v141, v141
	v_exp_f32_e32 v142, v142
	v_exp_f32_e32 v143, v143
	v_exp_f32_e32 v144, v144
	v_exp_f32_e32 v145, v145
	v_pk_add_f32 v[130:131], v[130:131], 1.0 op_sel_hi:[1,0]
	v_pk_add_f32 v[132:133], v[132:133], 1.0 op_sel_hi:[1,0]
	v_pk_add_f32 v[134:135], v[134:135], 1.0 op_sel_hi:[1,0]
	v_pk_add_f32 v[136:137], v[136:137], 1.0 op_sel_hi:[1,0]
	v_pk_add_f32 v[138:139], v[138:139], 1.0 op_sel_hi:[1,0]
	v_pk_add_f32 v[140:141], v[140:141], 1.0 op_sel_hi:[1,0]
	v_pk_add_f32 v[142:143], v[142:143], 1.0 op_sel_hi:[1,0]
	v_pk_add_f32 v[144:145], v[144:145], 1.0 op_sel_hi:[1,0]
	v_rcp_f32_e32 v130, v130
	v_rcp_f32_e32 v131, v131
	v_rcp_f32_e32 v132, v132
	v_rcp_f32_e32 v133, v133
	v_rcp_f32_e32 v134, v134
	v_rcp_f32_e32 v135, v135
	v_rcp_f32_e32 v136, v136
	v_rcp_f32_e32 v137, v137
	v_rcp_f32_e32 v138, v138
	v_rcp_f32_e32 v139, v139
	v_rcp_f32_e32 v140, v140
	v_rcp_f32_e32 v141, v141
	v_rcp_f32_e32 v142, v142
	v_rcp_f32_e32 v143, v143
	v_rcp_f32_e32 v144, v144
	v_rcp_f32_e32 v145, v145
	v_pk_fma_f32 v[130:131], v[130:131], 2.0, 1.0 op_sel_hi:[1,0,0] neg_lo:[1,0,0] neg_hi:[1,0,0]
	v_pk_fma_f32 v[132:133], v[132:133], 2.0, 1.0 op_sel_hi:[1,0,0] neg_lo:[1,0,0] neg_hi:[1,0,0]
	v_pk_fma_f32 v[134:135], v[134:135], 2.0, 1.0 op_sel_hi:[1,0,0] neg_lo:[1,0,0] neg_hi:[1,0,0]
	v_pk_fma_f32 v[136:137], v[136:137], 2.0, 1.0 op_sel_hi:[1,0,0] neg_lo:[1,0,0] neg_hi:[1,0,0]
	v_pk_fma_f32 v[138:139], v[138:139], 2.0, 1.0 op_sel_hi:[1,0,0] neg_lo:[1,0,0] neg_hi:[1,0,0]
	v_pk_fma_f32 v[140:141], v[140:141], 2.0, 1.0 op_sel_hi:[1,0,0] neg_lo:[1,0,0] neg_hi:[1,0,0]
	v_pk_fma_f32 v[142:143], v[142:143], 2.0, 1.0 op_sel_hi:[1,0,0] neg_lo:[1,0,0] neg_hi:[1,0,0]
	v_pk_fma_f32 v[144:145], v[144:145], 2.0, 1.0 op_sel_hi:[1,0,0] neg_lo:[1,0,0] neg_hi:[1,0,0]
	v_cvt_pk_f16_f32 v146, v130, v131
	v_cvt_pk_f16_f32 v147, v132, v133
	v_cvt_pk_f16_f32 v148, v134, v135
	v_cvt_pk_f16_f32 v149, v136, v137
	v_cvt_pk_f16_f32 v150, v138, v139
	v_cvt_pk_f16_f32 v151, v140, v141
	v_cvt_pk_f16_f32 v152, v142, v143
	v_cvt_pk_f16_f32 v153, v144, v145
	s_nop 1
	v_permlane32_swap_b32_e32 v146, v148
	v_permlane32_swap_b32_e32 v147, v149
	v_permlane32_swap_b32_e32 v150, v152
	v_permlane32_swap_b32_e32 v151, v153
	global_store_dwordx4 v157, v[146:149], s[32:33] sc1
	global_store_dwordx4 v157, v[150:153], s[32:33] offset:1024 sc1
	s_add_u32 s32, s32, 0x10000
	s_addc_u32 s33, s33, 0
	v_pk_fma_f32 v[130:131], v[114:115], s[4:5], v[66:67] op_sel_hi:[1,0,1]
	v_pk_fma_f32 v[132:133], v[116:117], s[4:5], v[68:69] op_sel_hi:[1,0,1]
	v_pk_fma_f32 v[134:135], v[118:119], s[4:5], v[70:71] op_sel_hi:[1,0,1]
	v_pk_fma_f32 v[136:137], v[120:121], s[4:5], v[72:73] op_sel_hi:[1,0,1]
	v_pk_fma_f32 v[138:139], v[122:123], s[4:5], v[74:75] op_sel_hi:[1,0,1]
	v_pk_fma_f32 v[140:141], v[124:125], s[4:5], v[76:77] op_sel_hi:[1,0,1]
	v_pk_fma_f32 v[142:143], v[126:127], s[4:5], v[78:79] op_sel_hi:[1,0,1]
	v_pk_fma_f32 v[144:145], v[128:129], s[4:5], v[80:81] op_sel_hi:[1,0,1]
	v_exp_f32_e32 v130, v130
	v_exp_f32_e32 v131, v131
	v_exp_f32_e32 v132, v132
	v_exp_f32_e32 v133, v133
	v_exp_f32_e32 v134, v134
	v_exp_f32_e32 v135, v135
	v_exp_f32_e32 v136, v136
	v_exp_f32_e32 v137, v137
	v_exp_f32_e32 v138, v138
	v_exp_f32_e32 v139, v139
	v_exp_f32_e32 v140, v140
	v_exp_f32_e32 v141, v141
	v_exp_f32_e32 v142, v142
	v_exp_f32_e32 v143, v143
	v_exp_f32_e32 v144, v144
	v_exp_f32_e32 v145, v145
	v_pk_add_f32 v[130:131], v[130:131], 1.0 op_sel_hi:[1,0]
	v_pk_add_f32 v[132:133], v[132:133], 1.0 op_sel_hi:[1,0]
	v_pk_add_f32 v[134:135], v[134:135], 1.0 op_sel_hi:[1,0]
	v_pk_add_f32 v[136:137], v[136:137], 1.0 op_sel_hi:[1,0]
	v_pk_add_f32 v[138:139], v[138:139], 1.0 op_sel_hi:[1,0]
	v_pk_add_f32 v[140:141], v[140:141], 1.0 op_sel_hi:[1,0]
	v_pk_add_f32 v[142:143], v[142:143], 1.0 op_sel_hi:[1,0]
	v_pk_add_f32 v[144:145], v[144:145], 1.0 op_sel_hi:[1,0]
	v_rcp_f32_e32 v130, v130
	v_rcp_f32_e32 v131, v131
	v_rcp_f32_e32 v132, v132
	v_rcp_f32_e32 v133, v133
	v_rcp_f32_e32 v134, v134
	v_rcp_f32_e32 v135, v135
	v_rcp_f32_e32 v136, v136
	v_rcp_f32_e32 v137, v137
	v_rcp_f32_e32 v138, v138
	v_rcp_f32_e32 v139, v139
	v_rcp_f32_e32 v140, v140
	v_rcp_f32_e32 v141, v141
	v_rcp_f32_e32 v142, v142
	v_rcp_f32_e32 v143, v143
	v_rcp_f32_e32 v144, v144
	v_rcp_f32_e32 v145, v145
	v_pk_fma_f32 v[130:131], v[130:131], 2.0, 1.0 op_sel_hi:[1,0,0] neg_lo:[1,0,0] neg_hi:[1,0,0]
	v_pk_fma_f32 v[132:133], v[132:133], 2.0, 1.0 op_sel_hi:[1,0,0] neg_lo:[1,0,0] neg_hi:[1,0,0]
	v_pk_fma_f32 v[134:135], v[134:135], 2.0, 1.0 op_sel_hi:[1,0,0] neg_lo:[1,0,0] neg_hi:[1,0,0]
	v_pk_fma_f32 v[136:137], v[136:137], 2.0, 1.0 op_sel_hi:[1,0,0] neg_lo:[1,0,0] neg_hi:[1,0,0]
	v_pk_fma_f32 v[138:139], v[138:139], 2.0, 1.0 op_sel_hi:[1,0,0] neg_lo:[1,0,0] neg_hi:[1,0,0]
	v_pk_fma_f32 v[140:141], v[140:141], 2.0, 1.0 op_sel_hi:[1,0,0] neg_lo:[1,0,0] neg_hi:[1,0,0]
	v_pk_fma_f32 v[142:143], v[142:143], 2.0, 1.0 op_sel_hi:[1,0,0] neg_lo:[1,0,0] neg_hi:[1,0,0]
	v_pk_fma_f32 v[144:145], v[144:145], 2.0, 1.0 op_sel_hi:[1,0,0] neg_lo:[1,0,0] neg_hi:[1,0,0]
	v_cvt_pk_f16_f32 v146, v130, v131
	v_cvt_pk_f16_f32 v147, v132, v133
	v_cvt_pk_f16_f32 v148, v134, v135
	v_cvt_pk_f16_f32 v149, v136, v137
	v_cvt_pk_f16_f32 v150, v138, v139
	v_cvt_pk_f16_f32 v151, v140, v141
	v_cvt_pk_f16_f32 v152, v142, v143
	v_cvt_pk_f16_f32 v153, v144, v145
	s_nop 1
	v_permlane32_swap_b32_e32 v146, v148
	v_permlane32_swap_b32_e32 v147, v149
	v_permlane32_swap_b32_e32 v150, v152
	v_permlane32_swap_b32_e32 v151, v153
	global_store_dwordx4 v157, v[146:149], s[32:33] sc1
	global_store_dwordx4 v157, v[150:153], s[32:33] offset:1024 sc1
	s_waitcnt vmcnt(11)
	v_cvt_pk_f16_f32 v168, v168, v169
	v_cvt_pk_f16_f32 v169, v170, v171
	ds_write_b64 v164, v[168:169] offset:0
	s_waitcnt vmcnt(10)
	v_cvt_pk_f16_f32 v172, v172, v173
	v_cvt_pk_f16_f32 v173, v174, v175
	ds_write_b64 v164, v[172:173] offset:64
	s_waitcnt vmcnt(9)
	v_cvt_pk_f16_f32 v176, v176, v177
	v_cvt_pk_f16_f32 v177, v178, v179
	ds_write_b64 v164, v[176:177] offset:128
	s_waitcnt vmcnt(8)
	v_cvt_pk_f16_f32 v180, v180, v181
	v_cvt_pk_f16_f32 v181, v182, v183
	ds_write_b64 v164, v[180:181] offset:192
	s_waitcnt lgkmcnt(0)
	s_barrier
	ds_read_b128 v[2:5], v166
	ds_read_b128 v[6:9], v166 offset:32
	ds_read_u16 v10, v167 offset:0
	ds_read_u16 v11, v167 offset:272
	ds_read_u16 v12, v167 offset:544
	ds_read_u16 v13, v167 offset:816
	ds_read_u16 v14, v167 offset:1088
	ds_read_u16 v15, v167 offset:1360
	ds_read_u16 v16, v167 offset:1632
	ds_read_u16 v17, v167 offset:1904
	s_waitcnt lgkmcnt(8)
	global_store_dwordx4 v157, v[2:5], s[36:37] sc1
	global_store_dwordx4 v157, v[6:9], s[36:37] offset:1024 sc1
	s_waitcnt lgkmcnt(0)
	v_lshl_or_b32 v10, v11, 16, v10
	v_lshl_or_b32 v11, v13, 16, v12
	v_lshl_or_b32 v12, v15, 16, v14
	v_lshl_or_b32 v13, v17, 16, v16
	global_store_dwordx4 v157, v[10:13], s[38:39] sc1
	ds_read_u16 v18, v167 offset:4352
	ds_read_u16 v19, v167 offset:4624
	ds_read_u16 v20, v167 offset:4896
	ds_read_u16 v21, v167 offset:5168
	ds_read_u16 v22, v167 offset:5440
	ds_read_u16 v23, v167 offset:5712
	ds_read_u16 v24, v167 offset:5984
	ds_read_u16 v25, v167 offset:6256
	s_waitcnt lgkmcnt(0)
	v_lshl_or_b32 v18, v19, 16, v18
	v_lshl_or_b32 v19, v21, 16, v20
	v_lshl_or_b32 v20, v23, 16, v22
	v_lshl_or_b32 v21, v25, 16, v24
	global_store_dwordx4 v157, v[18:21], s[38:39] offset:1024 sc1
	s_endpgm

	.amdhsa_kernel _Z6k_prepPKfS0_S0_S0_PDF16_S1_S1_S1_S0_S0_S0_
		.amdhsa_group_segment_fixed_size 33792
		.amdhsa_private_segment_fixed_size 0
		.amdhsa_kernarg_size 88
		.amdhsa_user_sgpr_count 2
		.amdhsa_user_sgpr_dispatch_ptr 0
		.amdhsa_user_sgpr_queue_ptr 0
		.amdhsa_user_sgpr_kernarg_segment_ptr 1
		.amdhsa_user_sgpr_dispatch_id 0
		.amdhsa_user_sgpr_kernarg_preload_length 0
		.amdhsa_user_sgpr_kernarg_preload_offset 0
		.amdhsa_user_sgpr_private_segment_size 0
		.amdhsa_uses_dynamic_stack 0
		.amdhsa_enable_private_segment 0
		.amdhsa_system_sgpr_workgroup_id_x 1
		.amdhsa_system_sgpr_workgroup_id_y 0
		.amdhsa_system_sgpr_workgroup_id_z 0
		.amdhsa_system_sgpr_workgroup_info 0
		.amdhsa_system_vgpr_workitem_id 0
		.amdhsa_next_free_vgpr 200
		.amdhsa_next_free_sgpr 96
		.amdhsa_accum_offset 184
		.amdhsa_reserve_vcc 1
		.amdhsa_float_round_mode_32 0
		.amdhsa_float_round_mode_16_64 0
		.amdhsa_float_denorm_mode_32 3
		.amdhsa_float_denorm_mode_16_64 3
		.amdhsa_dx10_clamp 1
		.amdhsa_ieee_mode 1
		.amdhsa_fp16_overflow 0
		.amdhsa_tg_split 0
		.amdhsa_exception_fp_ieee_invalid_op 0
		.amdhsa_exception_fp_denorm_src 0
		.amdhsa_exception_fp_ieee_div_zero 0
		.amdhsa_exception_fp_ieee_overflow 0
		.amdhsa_exception_fp_ieee_underflow 0
		.amdhsa_exception_fp_ieee_inexact 0
		.amdhsa_exception_int_div_zero 0
	.end_amdhsa_kernel

amdhsa.kernels:
  - .agpr_count:     16
    .args:
      - .actual_access:  read_only
        .address_space:  global
        .offset:         0
        .size:           8
        .value_kind:     global_buffer
      - .actual_access:  read_only
        .address_space:  global
        .offset:         8
        .size:           8
        .value_kind:     global_buffer
      - .actual_access:  read_only
        .address_space:  global
        .offset:         16
        .size:           8
        .value_kind:     global_buffer
      - .actual_access:  read_only
        .address_space:  global
        .offset:         24
        .size:           8
        .value_kind:     global_buffer
      - .actual_access:  write_only
        .address_space:  global
        .offset:         32
        .size:           8
        .value_kind:     global_buffer
      - .actual_access:  write_only
        .address_space:  global
        .offset:         40
        .size:           8
        .value_kind:     global_buffer
      - .actual_access:  write_only
        .address_space:  global
        .offset:         48
        .size:           8
        .value_kind:     global_buffer
      - .actual_access:  write_only
        .address_space:  global
        .offset:         56
        .size:           8
        .value_kind:     global_buffer
      - .actual_access:  read_only
        .address_space:  global
        .offset:         64
        .size:           8
        .value_kind:     global_buffer
      - .actual_access:  read_only
        .address_space:  global
        .offset:         72
        .size:           8
        .value_kind:     global_buffer
      - .actual_access:  read_only
        .address_space:  global
        .offset:         80
        .size:           8
        .value_kind:     global_buffer
    .group_segment_fixed_size: 33792
    .kernarg_segment_align: 8
    .kernarg_segment_size: 88
    .language:       OpenCL C
    .language_version:
      - 2
      - 0
    .max_flat_workgroup_size: 256
    .name:           _Z6k_prepPKfS0_S0_S0_PDF16_S1_S1_S1_S0_S0_S0_
    .private_segment_fixed_size: 0
    .sgpr_count:     22
    .sgpr_spill_count: 0
    .symbol:         _Z6k_prepPKfS0_S0_S0_PDF16_S1_S1_S1_S0_S0_S0_.kd
    .uniform_work_group_size: 1
    .uses_dynamic_stack: false
    .vgpr_count:     200
    .vgpr_spill_count: 0
    .wavefront_size: 64
  - .agpr_count:     0
    .args:
      - .actual_access:  read_only
        .address_space:  global
        .offset:         0
        .size:           8
        .value_kind:     global_buffer
      - .actual_access:  read_only
        .address_space:  global
        .offset:         8
        .size:           8
        .value_kind:     global_buffer
      - .actual_access:  read_only
        .address_space:  global
        .offset:         16
        .size:           8
        .value_kind:     global_buffer
      - .actual_access:  write_only
        .address_space:  global
        .offset:         24
        .size:           8
        .value_kind:     global_buffer
    .group_segment_fixed_size: 0
    .kernarg_segment_align: 8
    .kernarg_segment_size: 32
    .language:       OpenCL C
    .language_version:
      - 2
      - 0
    .max_flat_workgroup_size: 128
    .name:           _Z7k_finalPKfS0_S0_Pf
    .private_segment_fixed_size: 0
    .sgpr_count:     18
    .sgpr_spill_count: 0
    .symbol:         _Z7k_finalPKfS0_S0_Pf.kd
    .uniform_work_group_size: 1
    .uses_dynamic_stack: false
    .vgpr_count:     62
    .vgpr_spill_count: 0
    .wavefront_size: 64
  - .agpr_count:     0
    .args:
      - .actual_access:  read_only
        .address_space:  global
        .offset:         0
        .size:           8
        .value_kind:     global_buffer
      - .actual_access:  read_only
        .address_space:  global
        .offset:         8
        .size:           8
        .value_kind:     global_buffer
      - .actual_access:  read_only
        .address_space:  global
        .offset:         16
        .size:           8
        .value_kind:     global_buffer
      - .actual_access:  read_only
        .address_space:  global
        .offset:         24
        .size:           8
        .value_kind:     global_buffer
      - .actual_access:  read_only
        .address_space:  global
        .offset:         32
        .size:           8
        .value_kind:     global_buffer
      - .actual_access:  write_only
        .address_space:  global
        .offset:         40
        .size:           8
        .value_kind:     global_buffer
      - .actual_access:  write_only
        .address_space:  global
        .offset:         48
        .size:           8
        .value_kind:     global_buffer
      - .actual_access:  read_only
        .address_space:  global
        .offset:         56
        .size:           8
        .value_kind:     global_buffer
      - .actual_access:  read_only
        .address_space:  global
        .offset:         64
        .size:           8
        .value_kind:     global_buffer
    .group_segment_fixed_size: 33808
    .kernarg_segment_align: 8
    .kernarg_segment_size: 72
    .language:       OpenCL C
    .language_version:
      - 2
      - 0
    .max_flat_workgroup_size: 384
    .name:           _Z6k_gemmILi0EEvPKDF16_S1_PKfS3_S1_PDF16_PfS1_S5_
    .private_segment_fixed_size: 0
    .sgpr_count:     20
    .sgpr_spill_count: 0
    .symbol:         _Z6k_gemmILi0EEvPKDF16_S1_PKfS3_S1_PDF16_PfS1_S5_.kd
    .uniform_work_group_size: 1
    .uses_dynamic_stack: false
    .vgpr_count:     150
    .vgpr_spill_count: 0
    .wavefront_size: 64
  - .agpr_count:     0
    .args:
      - .actual_access:  read_only
        .address_space:  global
        .offset:         0
        .size:           8
        .value_kind:     global_buffer
      - .actual_access:  read_only
        .address_space:  global
        .offset:         8
        .size:           8
        .value_kind:     global_buffer
      - .actual_access:  read_only
        .address_space:  global
        .offset:         16
        .size:           8
        .value_kind:     global_buffer
      - .actual_access:  read_only
        .address_space:  global
        .offset:         24
        .size:           8
        .value_kind:     global_buffer
      - .actual_access:  read_only
        .address_space:  global
        .offset:         32
        .size:           8
        .value_kind:     global_buffer
      - .actual_access:  read_only
        .address_space:  global
        .offset:         40
        .size:           8
        .value_kind:     global_buffer
      - .actual_access:  read_only
        .address_space:  global
        .offset:         48
        .size:           8
        .value_kind:     global_buffer
      - .actual_access:  read_only
        .address_space:  global
        .offset:         56
        .size:           8
        .value_kind:     global_buffer
      - .actual_access:  write_only
        .address_space:  global
        .offset:         64
        .size:           8
        .value_kind:     global_buffer
    .group_segment_fixed_size: 50176
    .kernarg_segment_align: 8
    .kernarg_segment_size: 72
    .language:       OpenCL C
    .language_version:
      - 2
      - 0
    .max_flat_workgroup_size: 384
    .name:           _Z6k_gemmILi1EEvPKDF16_S1_PKfS3_S1_PDF16_PfS1_S5_
    .private_segment_fixed_size: 0
    .sgpr_count:     20
    .sgpr_spill_count: 0
    .symbol:         _Z6k_gemmILi1EEvPKDF16_S1_PKfS3_S1_PDF16_PfS1_S5_.kd
    .uniform_work_group_size: 1
    .uses_dynamic_stack: false
    .vgpr_count:     182
    .vgpr_spill_count: 0
    .wavefront_size: 64
